# speedup vs baseline: 1.0033x; 1.0033x over previous
_Z10cvt_kernelPKfPDF16_lS0_S1_lS0_S1_lS0_S1_lS0_S1_lPjS0_Pf:
	s_load_dwordx4 s[28:31], s[0:1], 0x0
	s_load_dwordx4 s[32:35], s[0:1], 0x18
	s_cmpk_lt_u32 s2, 0x80
	s_cbranch_scc1 .Lcvt_orig
	s_cmpk_ge_u32 s2, 0x1000
	s_cbranch_scc1 .Lcvt_orig
	v_lshlrev_b32_e32 v1, 5, v0
	v_lshlrev_b32_e32 v2, 4, v0
	s_cmpk_ge_u32 s2, 0x800
	s_cbranch_scc1 .Lcvt_fw
	s_lshl_b32 s8, s2, 13
	s_lshl_b32 s9, s2, 12
	s_waitcnt lgkmcnt(0)
	s_add_u32 s4, s28, s8
	s_addc_u32 s5, s29, 0
	s_add_u32 s6, s30, s9
	s_addc_u32 s7, s31, 0
	global_load_dwordx4 v[4:7], v1, s[4:5] nt
	global_load_dwordx4 v[8:11], v1, s[4:5] offset:16 nt
	s_waitcnt vmcnt(1)
	v_cvt_pk_f16_f32 v12, v4, v5
	v_cvt_pk_f16_f32 v13, v6, v7
	s_waitcnt vmcnt(0)
	v_cvt_pk_f16_f32 v14, v8, v9
	v_cvt_pk_f16_f32 v15, v10, v11
	global_store_dwordx4 v2, v[12:15], s[6:7]
	s_endpgm
.Lcvt_fw:
	s_sub_u32 s3, s2, 0x800
	s_lshl_b32 s8, s3, 13
	s_lshl_b32 s9, s3, 12
	s_mov_b32 s10, 0x41800000
	s_mov_b32 s11, 0x41800000
	s_waitcnt lgkmcnt(0)
	s_add_u32 s4, s32, s8
	s_addc_u32 s5, s33, 0
	s_add_u32 s6, s34, s9
	s_addc_u32 s7, s35, 0
	global_load_dwordx4 v[4:7], v1, s[4:5] nt
	global_load_dwordx4 v[8:11], v1, s[4:5] offset:16 nt
	s_waitcnt vmcnt(1)
	v_pk_mul_f32 v[4:5], v[4:5], s[10:11]
	v_pk_mul_f32 v[6:7], v[6:7], s[10:11]
	s_waitcnt vmcnt(0)
	v_pk_mul_f32 v[8:9], v[8:9], s[10:11]
	v_pk_mul_f32 v[10:11], v[10:11], s[10:11]
	v_cvt_pk_f16_f32 v12, v4, v5
	v_cvt_pk_f16_f32 v13, v6, v7
	v_cvt_pk_f16_f32 v14, v8, v9
	v_cvt_pk_f16_f32 v15, v10, v11
	global_store_dwordx4 v2, v[12:15], s[6:7]
	s_endpgm
